# code placement: fp8 GEMM loop heads (P6, P8, P9 gate/up) aligned to 64 bytes with .p2align 6 (pad executed once per loop entry)
# speedup vs baseline: 1.0101x; 1.0028x over previous
.LBB0_925:
	s_addk_i32 s33, 0x100
	s_add_i32 s79, s79, 2
	s_cmpk_eq_i32 s33, 0xf00
	s_cbranch_scc1 .LBB0_932
	.p2align 6

.LBB0_1228:
	s_add_i32 s28, s61, 0x180
	s_add_i32 s29, s60, 0x180
	s_waitcnt lgkmcnt(0)
	s_barrier
	s_setprio 1
	v_mfma_scale_f32_16x16x128_f8f6f4 v[128:131], v[24:31], v[56:63], 0, v201, v201 op_sel_hi:[0,0,0]
	v_mfma_scale_f32_16x16x128_f8f6f4 v[124:127], v[16:23], v[56:63], 0, v201, v201 op_sel_hi:[0,0,0]
	v_mfma_scale_f32_16x16x128_f8f6f4 v[120:123], v[24:31], v[48:55], 0, v201, v201 op_sel_hi:[0,0,0]
	v_mfma_scale_f32_16x16x128_f8f6f4 v[116:119], v[16:23], v[48:55], 0, v201, v201 op_sel_hi:[0,0,0]
	v_mfma_scale_f32_16x16x128_f8f6f4 v[112:115], v[24:31], v[40:47], 0, v201, v201 op_sel_hi:[0,0,0]
	v_mfma_scale_f32_16x16x128_f8f6f4 v[108:111], v[16:23], v[40:47], 0, v201, v201 op_sel_hi:[0,0,0]
	v_mfma_scale_f32_16x16x128_f8f6f4 v[104:107], v[24:31], v[32:39], 0, v201, v201 op_sel_hi:[0,0,0]
	v_mfma_scale_f32_16x16x128_f8f6f4 v[100:103], v[16:23], v[32:39], 0, v201, v201 op_sel_hi:[0,0,0]
	s_setprio 0
	s_setprio 1
	v_mfma_scale_f32_16x16x128_f8f6f4 v[96:99], v[8:15], v[56:63], 0, v201, v201 op_sel_hi:[0,0,0]
	v_mfma_scale_f32_16x16x128_f8f6f4 v[92:95], v[0:7], v[56:63], 0, v201, v201 op_sel_hi:[0,0,0]
	v_mfma_scale_f32_16x16x128_f8f6f4 v[88:91], v[8:15], v[48:55], 0, v201, v201 op_sel_hi:[0,0,0]
	v_mfma_scale_f32_16x16x128_f8f6f4 v[84:87], v[0:7], v[48:55], 0, v201, v201 op_sel_hi:[0,0,0]
	v_mfma_scale_f32_16x16x128_f8f6f4 v[80:83], v[8:15], v[40:47], 0, v201, v201 op_sel_hi:[0,0,0]
	v_mfma_scale_f32_16x16x128_f8f6f4 v[76:79], v[0:7], v[40:47], 0, v201, v201 op_sel_hi:[0,0,0]
	v_mfma_scale_f32_16x16x128_f8f6f4 v[72:75], v[8:15], v[32:39], 0, v201, v201 op_sel_hi:[0,0,0]
	v_mfma_scale_f32_16x16x128_f8f6f4 v[68:71], v[0:7], v[32:39], 0, v201, v201 op_sel_hi:[0,0,0]
	s_setprio 0
	s_barrier
	ds_read_b128 v[24:27], v205 offset:0x8000
	ds_read_b128 v[28:31], v205 offset:0x8400
	ds_read_b128 v[16:19], v205 offset:0x8800
	ds_read_b128 v[20:23], v205 offset:0x8c00
	ds_read_b128 v[32:35], v204 offset:0x8000
	ds_read_b128 v[36:39], v204 offset:0x8400
	ds_read_b128 v[40:43], v204 offset:0x8800
	ds_read_b128 v[44:47], v204 offset:0x8c00
	ds_read_b128 v[48:51], v204 offset:0x9000
	ds_read_b128 v[52:55], v204 offset:0x9400
	ds_read_b128 v[56:59], v204 offset:0x9800
	ds_read_b128 v[60:63], v204 offset:0x9c00
	ds_read_b128 v[8:11], v205 offset:0xc000
	ds_read_b128 v[12:15], v205 offset:0xc400
	ds_read_b128 v[0:3], v205 offset:0xc800
	ds_read_b128 v[4:7], v205 offset:0xcc00
	s_mov_b32 m0, s44
	s_nop 0
	buffer_load_dwordx4 v216, s[4:7], s33 offen lds
	s_mov_b32 m0, s45
	s_nop 0
	buffer_load_dwordx4 v215, s[4:7], s33 offen lds
	s_waitcnt vmcnt(8)
	s_waitcnt lgkmcnt(4)
	s_barrier
	s_setprio 1
	v_mfma_scale_f32_16x16x128_f8f6f4 v[192:195], v[24:31], v[32:39], v[192:195], v201, v201 op_sel_hi:[0,0,0]
	v_mfma_scale_f32_16x16x128_f8f6f4 v[188:191], v[16:23], v[32:39], v[188:191], v201, v201 op_sel_hi:[0,0,0]
	v_mfma_scale_f32_16x16x128_f8f6f4 v[184:187], v[24:31], v[40:47], v[184:187], v201, v201 op_sel_hi:[0,0,0]
	v_mfma_scale_f32_16x16x128_f8f6f4 v[180:183], v[16:23], v[40:47], v[180:183], v201, v201 op_sel_hi:[0,0,0]
	v_mfma_scale_f32_16x16x128_f8f6f4 v[176:179], v[24:31], v[48:55], v[176:179], v201, v201 op_sel_hi:[0,0,0]
	v_mfma_scale_f32_16x16x128_f8f6f4 v[172:175], v[16:23], v[48:55], v[172:175], v201, v201 op_sel_hi:[0,0,0]
	v_mfma_scale_f32_16x16x128_f8f6f4 v[168:171], v[24:31], v[56:63], v[168:171], v201, v201 op_sel_hi:[0,0,0]
	v_mfma_scale_f32_16x16x128_f8f6f4 v[164:167], v[16:23], v[56:63], v[164:167], v201, v201 op_sel_hi:[0,0,0]
	s_setprio 0
	s_setprio 1
	s_waitcnt lgkmcnt(2)
	v_mfma_scale_f32_16x16x128_f8f6f4 v[160:163], v[8:15], v[32:39], v[160:163], v201, v201 op_sel_hi:[0,0,0]
	s_waitcnt lgkmcnt(0)
	v_mfma_scale_f32_16x16x128_f8f6f4 v[156:159], v[0:7], v[32:39], v[156:159], v201, v201 op_sel_hi:[0,0,0]
	v_mfma_scale_f32_16x16x128_f8f6f4 v[152:155], v[8:15], v[40:47], v[152:155], v201, v201 op_sel_hi:[0,0,0]
	v_mfma_scale_f32_16x16x128_f8f6f4 v[148:151], v[0:7], v[40:47], v[148:151], v201, v201 op_sel_hi:[0,0,0]
	v_mfma_scale_f32_16x16x128_f8f6f4 v[144:147], v[8:15], v[48:55], v[144:147], v201, v201 op_sel_hi:[0,0,0]
	v_mfma_scale_f32_16x16x128_f8f6f4 v[140:143], v[0:7], v[48:55], v[140:143], v201, v201 op_sel_hi:[0,0,0]
	v_mfma_scale_f32_16x16x128_f8f6f4 v[136:139], v[8:15], v[56:63], v[136:139], v201, v201 op_sel_hi:[0,0,0]
	v_mfma_scale_f32_16x16x128_f8f6f4 v[132:135], v[0:7], v[56:63], v[132:135], v201, v201 op_sel_hi:[0,0,0]
	s_setprio 0
	s_barrier
	ds_read_b128 v[32:35], v204 offset:0xc000
	ds_read_b128 v[36:39], v204 offset:0xc400
	ds_read_b128 v[40:43], v204 offset:0xc800
	ds_read_b128 v[44:47], v204 offset:0xcc00
	ds_read_b128 v[48:51], v204 offset:0xd000
	ds_read_b128 v[52:55], v204 offset:0xd400
	ds_read_b128 v[56:59], v204 offset:0xd800
	ds_read_b128 v[60:63], v204 offset:0xdc00
	s_mov_b32 m0, s48
	s_mov_b32 s10, s6
	s_mov_b32 s11, s7
	buffer_load_dwordx4 v203, s[8:11], s29 offen lds
	s_add_i32 s29, s60, 0x80180
	s_mov_b32 m0, s49
	s_nop 0
	buffer_load_dwordx4 v203, s[8:11], s29 offen lds
	s_add_i32 s29, s60, 0x8180
	s_mov_b32 m0, s62
	s_nop 0
	buffer_load_dwordx4 v203, s[8:11], s29 offen lds
	s_add_i32 s29, s60, 0x88180
	s_mov_b32 m0, s63
	s_nop 0
	buffer_load_dwordx4 v203, s[8:11], s29 offen lds
	s_mov_b32 m0, s50
	s_nop 0
	buffer_load_dwordx4 v214, s[4:7], s28 offen lds
	s_mov_b32 m0, s51
	s_nop 0
	buffer_load_dwordx4 v217, s[4:7], s28 offen lds
	s_waitcnt vmcnt(8)
	s_waitcnt lgkmcnt(0)
	s_barrier
	s_setprio 1
	v_mfma_scale_f32_16x16x128_f8f6f4 v[128:131], v[24:31], v[32:39], v[128:131], v201, v201 op_sel_hi:[0,0,0]
	v_mfma_scale_f32_16x16x128_f8f6f4 v[124:127], v[16:23], v[32:39], v[124:127], v201, v201 op_sel_hi:[0,0,0]
	v_mfma_scale_f32_16x16x128_f8f6f4 v[120:123], v[24:31], v[40:47], v[120:123], v201, v201 op_sel_hi:[0,0,0]
	v_mfma_scale_f32_16x16x128_f8f6f4 v[116:119], v[16:23], v[40:47], v[116:119], v201, v201 op_sel_hi:[0,0,0]
	v_mfma_scale_f32_16x16x128_f8f6f4 v[112:115], v[24:31], v[48:55], v[112:115], v201, v201 op_sel_hi:[0,0,0]
	v_mfma_scale_f32_16x16x128_f8f6f4 v[108:111], v[16:23], v[48:55], v[108:111], v201, v201 op_sel_hi:[0,0,0]
	v_mfma_scale_f32_16x16x128_f8f6f4 v[104:107], v[24:31], v[56:63], v[104:107], v201, v201 op_sel_hi:[0,0,0]
	v_mfma_scale_f32_16x16x128_f8f6f4 v[100:103], v[16:23], v[56:63], v[100:103], v201, v201 op_sel_hi:[0,0,0]
	s_setprio 0
	s_setprio 1
	v_mfma_scale_f32_16x16x128_f8f6f4 v[96:99], v[8:15], v[32:39], v[96:99], v201, v201 op_sel_hi:[0,0,0]
	v_mfma_scale_f32_16x16x128_f8f6f4 v[92:95], v[0:7], v[32:39], v[92:95], v201, v201 op_sel_hi:[0,0,0]
	v_mfma_scale_f32_16x16x128_f8f6f4 v[88:91], v[8:15], v[40:47], v[88:91], v201, v201 op_sel_hi:[0,0,0]
	v_mfma_scale_f32_16x16x128_f8f6f4 v[84:87], v[0:7], v[40:47], v[84:87], v201, v201 op_sel_hi:[0,0,0]
	v_mfma_scale_f32_16x16x128_f8f6f4 v[80:83], v[8:15], v[48:55], v[80:83], v201, v201 op_sel_hi:[0,0,0]
	v_mfma_scale_f32_16x16x128_f8f6f4 v[76:79], v[0:7], v[48:55], v[76:79], v201, v201 op_sel_hi:[0,0,0]
	v_mfma_scale_f32_16x16x128_f8f6f4 v[72:75], v[8:15], v[56:63], v[72:75], v201, v201 op_sel_hi:[0,0,0]
	v_mfma_scale_f32_16x16x128_f8f6f4 v[68:71], v[0:7], v[56:63], v[68:71], v201, v201 op_sel_hi:[0,0,0]
	s_setprio 0
	s_barrier
	s_waitcnt vmcnt(16)
	v_mbcnt_lo_u32_b32 v0, -1, 0
	v_mbcnt_hi_u32_b32 v0, -1, v0
	s_add_i32 s29, s60, 0x200
	v_lshl_add_u32 v0, v0, 4, s37
	v_ashrrev_i32_e32 v1, 31, v0
	v_lshrrev_b32_e32 v1, 22, v1
	v_add_u32_e32 v1, v0, v1
	v_ashrrev_i32_e32 v1, 10, v1
	v_mul_i32_i24_e32 v2, 0x400, v1
	v_sub_u32_e32 v2, v0, v2
	v_lshrrev_b32_e32 v3, 4, v2
	v_bitop3_b32 v3, v3, v2, 32 bitop3:0x6c
	v_ashrrev_i32_e32 v2, 31, v2
	v_lshrrev_b32_e32 v2, 26, v2
	v_add_u32_e32 v2, v3, v2
	v_and_b32_e32 v2, 0xc0, v2
	v_add_u32_e32 v0, 0x2000, v0
	v_sub_u32_e32 v2, v3, v2
	v_ashrrev_i32_e32 v3, 31, v0
	v_lshrrev_b32_e32 v3, 22, v3
	v_add_u32_e32 v3, v0, v3
	v_ashrrev_i32_e32 v3, 10, v3
	v_mul_i32_i24_e32 v4, 0x400, v3
	v_sub_u32_e32 v0, v0, v4
	v_lshrrev_b32_e32 v4, 4, v0
	v_bitop3_b32 v4, v4, v0, 32 bitop3:0x6c
	v_ashrrev_i32_e32 v0, 31, v0
	v_lshrrev_b32_e32 v0, 26, v0
	v_add_u32_e32 v0, v4, v0
	v_and_b32_e32 v0, 0xffc0, v0
	v_sub_u32_e32 v0, v4, v0
	v_lshrrev_b16_e32 v4, 7, v0
	v_and_b32_e32 v4, 1, v4
	v_add_u16_e32 v0, v0, v4
	v_lshlrev_b32_e32 v1, 5, v1
	v_ashrrev_i16_sdwa v2, v202, sext(v2) dst_sel:DWORD dst_unused:UNUSED_PAD src0_sel:DWORD src1_sel:BYTE_0
	v_lshlrev_b32_e32 v3, 5, v3
	v_ashrrev_i16_sdwa v0, v202, sext(v0) dst_sel:DWORD dst_unused:UNUSED_PAD src0_sel:DWORD src1_sel:BYTE_0
	v_and_b32_e32 v1, 32, v1
	v_bfe_i32 v2, v2, 0, 16
	v_and_b32_e32 v3, 32, v3
	v_bfe_i32 v0, v0, 0, 16
	v_add_lshl_u32 v1, v1, v2, 1
	v_add_lshl_u32 v0, v3, v0, 1
	v_lshl_add_u32 v32, v231, 12, v1
	v_lshl_add_u32 v33, v228, 12, v0
	v_lshl_add_u32 v34, v229, 12, v1
	v_lshl_add_u32 v35, v230, 12, v0
	s_mov_b32 s33, 0
	.p2align 6

.LBB0_1329:
	s_add_i32 s36, s89, 0x180
	s_add_i32 s37, s61, 0x180
	s_waitcnt lgkmcnt(0)
	s_barrier
	s_setprio 1
	v_mfma_scale_f32_16x16x128_f8f6f4 v[128:131], v[24:31], v[56:63], 0, v198, v198 op_sel_hi:[0,0,0]
	v_mfma_scale_f32_16x16x128_f8f6f4 v[124:127], v[16:23], v[56:63], 0, v198, v198 op_sel_hi:[0,0,0]
	v_mfma_scale_f32_16x16x128_f8f6f4 v[120:123], v[24:31], v[48:55], 0, v198, v198 op_sel_hi:[0,0,0]
	v_mfma_scale_f32_16x16x128_f8f6f4 v[116:119], v[16:23], v[48:55], 0, v198, v198 op_sel_hi:[0,0,0]
	v_mfma_scale_f32_16x16x128_f8f6f4 v[112:115], v[24:31], v[40:47], 0, v198, v198 op_sel_hi:[0,0,0]
	v_mfma_scale_f32_16x16x128_f8f6f4 v[108:111], v[16:23], v[40:47], 0, v198, v198 op_sel_hi:[0,0,0]
	v_mfma_scale_f32_16x16x128_f8f6f4 v[104:107], v[24:31], v[32:39], 0, v198, v198 op_sel_hi:[0,0,0]
	v_mfma_scale_f32_16x16x128_f8f6f4 v[100:103], v[16:23], v[32:39], 0, v198, v198 op_sel_hi:[0,0,0]
	s_setprio 0
	s_setprio 1
	v_mfma_scale_f32_16x16x128_f8f6f4 v[96:99], v[8:15], v[56:63], 0, v198, v198 op_sel_hi:[0,0,0]
	v_mfma_scale_f32_16x16x128_f8f6f4 v[92:95], v[0:7], v[56:63], 0, v198, v198 op_sel_hi:[0,0,0]
	v_mfma_scale_f32_16x16x128_f8f6f4 v[88:91], v[8:15], v[48:55], 0, v198, v198 op_sel_hi:[0,0,0]
	v_mfma_scale_f32_16x16x128_f8f6f4 v[84:87], v[0:7], v[48:55], 0, v198, v198 op_sel_hi:[0,0,0]
	v_mfma_scale_f32_16x16x128_f8f6f4 v[80:83], v[8:15], v[40:47], 0, v198, v198 op_sel_hi:[0,0,0]
	v_mfma_scale_f32_16x16x128_f8f6f4 v[76:79], v[0:7], v[40:47], 0, v198, v198 op_sel_hi:[0,0,0]
	v_mfma_scale_f32_16x16x128_f8f6f4 v[72:75], v[8:15], v[32:39], 0, v198, v198 op_sel_hi:[0,0,0]
	v_mfma_scale_f32_16x16x128_f8f6f4 v[68:71], v[0:7], v[32:39], 0, v198, v198 op_sel_hi:[0,0,0]
	s_setprio 0
	s_barrier
	ds_read_b128 v[24:27], v202 offset:0x8000
	ds_read_b128 v[28:31], v202 offset:0x8400
	ds_read_b128 v[16:19], v202 offset:0x8800
	ds_read_b128 v[20:23], v202 offset:0x8c00
	ds_read_b128 v[32:35], v201 offset:0x8000
	ds_read_b128 v[36:39], v201 offset:0x8400
	ds_read_b128 v[40:43], v201 offset:0x8800
	ds_read_b128 v[44:47], v201 offset:0x8c00
	ds_read_b128 v[48:51], v201 offset:0x9000
	ds_read_b128 v[52:55], v201 offset:0x9400
	ds_read_b128 v[56:59], v201 offset:0x9800
	ds_read_b128 v[60:63], v201 offset:0x9c00
	ds_read_b128 v[8:11], v202 offset:0xc000
	ds_read_b128 v[12:15], v202 offset:0xc400
	ds_read_b128 v[0:3], v202 offset:0xc800
	ds_read_b128 v[4:7], v202 offset:0xcc00
	s_mov_b32 m0, s50
	s_nop 0
	buffer_load_dwordx4 v207, s[4:7], s33 offen lds
	s_mov_b32 m0, s51
	s_nop 0
	buffer_load_dwordx4 v206, s[4:7], s33 offen lds
	s_waitcnt vmcnt(8)
	s_waitcnt lgkmcnt(4)
	s_barrier
	s_setprio 1
	v_mfma_scale_f32_16x16x128_f8f6f4 v[192:195], v[24:31], v[32:39], v[192:195], v198, v198 op_sel_hi:[0,0,0]
	v_mfma_scale_f32_16x16x128_f8f6f4 v[188:191], v[16:23], v[32:39], v[188:191], v198, v198 op_sel_hi:[0,0,0]
	v_mfma_scale_f32_16x16x128_f8f6f4 v[184:187], v[24:31], v[40:47], v[184:187], v198, v198 op_sel_hi:[0,0,0]
	v_mfma_scale_f32_16x16x128_f8f6f4 v[180:183], v[16:23], v[40:47], v[180:183], v198, v198 op_sel_hi:[0,0,0]
	v_mfma_scale_f32_16x16x128_f8f6f4 v[176:179], v[24:31], v[48:55], v[176:179], v198, v198 op_sel_hi:[0,0,0]
	v_mfma_scale_f32_16x16x128_f8f6f4 v[172:175], v[16:23], v[48:55], v[172:175], v198, v198 op_sel_hi:[0,0,0]
	v_mfma_scale_f32_16x16x128_f8f6f4 v[168:171], v[24:31], v[56:63], v[168:171], v198, v198 op_sel_hi:[0,0,0]
	v_mfma_scale_f32_16x16x128_f8f6f4 v[164:167], v[16:23], v[56:63], v[164:167], v198, v198 op_sel_hi:[0,0,0]
	s_setprio 0
	s_setprio 1
	s_waitcnt lgkmcnt(2)
	v_mfma_scale_f32_16x16x128_f8f6f4 v[160:163], v[8:15], v[32:39], v[160:163], v198, v198 op_sel_hi:[0,0,0]
	s_waitcnt lgkmcnt(0)
	v_mfma_scale_f32_16x16x128_f8f6f4 v[156:159], v[0:7], v[32:39], v[156:159], v198, v198 op_sel_hi:[0,0,0]
	v_mfma_scale_f32_16x16x128_f8f6f4 v[152:155], v[8:15], v[40:47], v[152:155], v198, v198 op_sel_hi:[0,0,0]
	v_mfma_scale_f32_16x16x128_f8f6f4 v[148:151], v[0:7], v[40:47], v[148:151], v198, v198 op_sel_hi:[0,0,0]
	v_mfma_scale_f32_16x16x128_f8f6f4 v[144:147], v[8:15], v[48:55], v[144:147], v198, v198 op_sel_hi:[0,0,0]
	v_mfma_scale_f32_16x16x128_f8f6f4 v[140:143], v[0:7], v[48:55], v[140:143], v198, v198 op_sel_hi:[0,0,0]
	v_mfma_scale_f32_16x16x128_f8f6f4 v[136:139], v[8:15], v[56:63], v[136:139], v198, v198 op_sel_hi:[0,0,0]
	v_mfma_scale_f32_16x16x128_f8f6f4 v[132:135], v[0:7], v[56:63], v[132:135], v198, v198 op_sel_hi:[0,0,0]
	s_setprio 0
	s_barrier
	ds_read_b128 v[32:35], v201 offset:0xc000
	ds_read_b128 v[36:39], v201 offset:0xc400
	ds_read_b128 v[40:43], v201 offset:0xc800
	ds_read_b128 v[44:47], v201 offset:0xcc00
	ds_read_b128 v[48:51], v201 offset:0xd000
	ds_read_b128 v[52:55], v201 offset:0xd400
	ds_read_b128 v[56:59], v201 offset:0xd800
	ds_read_b128 v[60:63], v201 offset:0xdc00
	s_mov_b32 m0, s64
	s_mov_b32 s10, s6
	s_mov_b32 s11, s7
	buffer_load_dwordx4 v200, s[8:11], s37 offen lds
	s_add_i32 s33, s61, 0x80180
	s_mov_b32 m0, s65
	s_nop 0
	buffer_load_dwordx4 v200, s[8:11], s33 offen lds
	s_add_i32 s33, s61, 0x8180
	s_mov_b32 m0, s70
	s_nop 0
	buffer_load_dwordx4 v200, s[8:11], s33 offen lds
	s_add_i32 s33, s61, 0x88180
	s_mov_b32 m0, s71
	s_nop 0
	buffer_load_dwordx4 v200, s[8:11], s33 offen lds
	s_mov_b32 m0, s68
	s_nop 0
	buffer_load_dwordx4 v205, s[4:7], s36 offen lds
	s_mov_b32 m0, s69
	s_nop 0
	buffer_load_dwordx4 v208, s[4:7], s36 offen lds
	s_waitcnt vmcnt(8)
	s_waitcnt lgkmcnt(0)
	s_barrier
	s_setprio 1
	v_mfma_scale_f32_16x16x128_f8f6f4 v[128:131], v[24:31], v[32:39], v[128:131], v198, v198 op_sel_hi:[0,0,0]
	v_mfma_scale_f32_16x16x128_f8f6f4 v[124:127], v[16:23], v[32:39], v[124:127], v198, v198 op_sel_hi:[0,0,0]
	v_mfma_scale_f32_16x16x128_f8f6f4 v[120:123], v[24:31], v[40:47], v[120:123], v198, v198 op_sel_hi:[0,0,0]
	v_mfma_scale_f32_16x16x128_f8f6f4 v[116:119], v[16:23], v[40:47], v[116:119], v198, v198 op_sel_hi:[0,0,0]
	v_mfma_scale_f32_16x16x128_f8f6f4 v[112:115], v[24:31], v[48:55], v[112:115], v198, v198 op_sel_hi:[0,0,0]
	v_mfma_scale_f32_16x16x128_f8f6f4 v[108:111], v[16:23], v[48:55], v[108:111], v198, v198 op_sel_hi:[0,0,0]
	v_mfma_scale_f32_16x16x128_f8f6f4 v[104:107], v[24:31], v[56:63], v[104:107], v198, v198 op_sel_hi:[0,0,0]
	v_mfma_scale_f32_16x16x128_f8f6f4 v[100:103], v[16:23], v[56:63], v[100:103], v198, v198 op_sel_hi:[0,0,0]
	s_setprio 0
	s_setprio 1
	v_mfma_scale_f32_16x16x128_f8f6f4 v[96:99], v[8:15], v[32:39], v[96:99], v198, v198 op_sel_hi:[0,0,0]
	v_mfma_scale_f32_16x16x128_f8f6f4 v[92:95], v[0:7], v[32:39], v[92:95], v198, v198 op_sel_hi:[0,0,0]
	v_mfma_scale_f32_16x16x128_f8f6f4 v[88:91], v[8:15], v[40:47], v[88:91], v198, v198 op_sel_hi:[0,0,0]
	v_mfma_scale_f32_16x16x128_f8f6f4 v[84:87], v[0:7], v[40:47], v[84:87], v198, v198 op_sel_hi:[0,0,0]
	v_mfma_scale_f32_16x16x128_f8f6f4 v[80:83], v[8:15], v[48:55], v[80:83], v198, v198 op_sel_hi:[0,0,0]
	v_mfma_scale_f32_16x16x128_f8f6f4 v[76:79], v[0:7], v[48:55], v[76:79], v198, v198 op_sel_hi:[0,0,0]
	v_mfma_scale_f32_16x16x128_f8f6f4 v[72:75], v[8:15], v[56:63], v[72:75], v198, v198 op_sel_hi:[0,0,0]
	v_mfma_scale_f32_16x16x128_f8f6f4 v[68:71], v[0:7], v[56:63], v[68:71], v198, v198 op_sel_hi:[0,0,0]
	s_setprio 0
	s_barrier
	s_waitcnt vmcnt(16)
	v_mbcnt_lo_u32_b32 v0, -1, 0
	v_mbcnt_hi_u32_b32 v0, -1, v0
	s_add_i32 s33, s61, 0x200
	v_lshl_add_u32 v0, v0, 4, s40
	v_ashrrev_i32_e32 v1, 31, v0
	v_lshrrev_b32_e32 v1, 22, v1
	v_add_u32_e32 v1, v0, v1
	v_ashrrev_i32_e32 v1, 10, v1
	v_mul_i32_i24_e32 v2, 0x400, v1
	v_sub_u32_e32 v2, v0, v2
	v_lshrrev_b32_e32 v3, 4, v2
	v_bitop3_b32 v3, v3, v2, 32 bitop3:0x6c
	v_ashrrev_i32_e32 v2, 31, v2
	v_lshrrev_b32_e32 v2, 26, v2
	v_add_u32_e32 v2, v3, v2
	v_and_b32_e32 v2, 0xc0, v2
	v_add_u32_e32 v0, 0x2000, v0
	v_sub_u32_e32 v2, v3, v2
	v_ashrrev_i32_e32 v3, 31, v0
	v_lshrrev_b32_e32 v3, 22, v3
	v_add_u32_e32 v3, v0, v3
	v_ashrrev_i32_e32 v3, 10, v3
	v_mul_i32_i24_e32 v4, 0x400, v3
	v_sub_u32_e32 v0, v0, v4
	v_lshrrev_b32_e32 v4, 4, v0
	v_bitop3_b32 v4, v4, v0, 32 bitop3:0x6c
	v_ashrrev_i32_e32 v0, 31, v0
	v_lshrrev_b32_e32 v0, 26, v0
	v_add_u32_e32 v0, v4, v0
	v_and_b32_e32 v0, 0xffc0, v0
	v_sub_u32_e32 v0, v4, v0
	v_lshrrev_b16_e32 v4, 7, v0
	v_and_b32_e32 v4, 1, v4
	v_add_u16_e32 v0, v0, v4
	v_lshlrev_b32_e32 v1, 5, v1
	v_ashrrev_i16_sdwa v2, v199, sext(v2) dst_sel:DWORD dst_unused:UNUSED_PAD src0_sel:DWORD src1_sel:BYTE_0
	v_lshlrev_b32_e32 v3, 5, v3
	v_ashrrev_i16_sdwa v0, v199, sext(v0) dst_sel:DWORD dst_unused:UNUSED_PAD src0_sel:DWORD src1_sel:BYTE_0
	v_and_b32_e32 v1, 32, v1
	v_bfe_i32 v2, v2, 0, 16
	v_and_b32_e32 v3, 32, v3
	v_bfe_i32 v0, v0, 0, 16
	v_add_lshl_u32 v1, v1, v2, 1
	v_add_lshl_u32 v0, v3, v0, 1
	v_lshl_add_u32 v32, v220, 12, v1
	v_lshl_add_u32 v33, v217, 12, v0
	v_lshl_add_u32 v34, v218, 12, v1
	v_lshl_add_u32 v35, v219, 12, v0
	s_mov_b32 s37, 0
	.p2align 6
